# v119 + P3 Q-row loads nt (read once per unit; streaming hint)
# speedup vs baseline: 1.0090x; 1.0090x over previous
; __device__ __forceinline__ void attn_phase_mfma(Frame& F) {
;     ...
;     for (int rep = 0; rep < 2; ++rep) {
;         const int j = blockIdx.x, bg = j >> 5, i = j & 31, qb = rep == 0 ? 63 - i : i, b = bg >> 1, g = bg & 1, h = 4 * g + hr;
;         const int q0 = qb * 32, tq = q0 + c; const size_t row_q = (size_t)(b * SEQ + tq);
;         bf16x8 qf[8];
; #pragma unroll
;         for (int ks = 0; ks < 8; ++ks) qf[ks] = *(const bf16x8*)(F.PROJ + row_q * INWP + O_Q + h * HD + 16 * ks + 8 * hh);
;         f32x16 o[4];
; #pragma unroll
;         for (int db = 0; db < 4; ++db)
; #pragma unroll
;             for (int r = 0; r < 16; ++r) o[db][r] = 0.f;
;         float m = -INFINITY, l = 0.f;
;         const float bfar = LUT[h * 132 + 128];
;         const int nsteps = (qb + 2) >> 1;
;         const bf16* kvb = F.PROJ + (size_t)(b * SEQ) * INWP + g * HD;
;         v4u sk[2], sv[2]; unsigned mw = 0u, mwn = 0u;
;     ...
;         if (grp <= qb) { AT_LOAD_TILE(grp); AT_WRITE_TILE(0); mw = mwn; }
;         if (grp + 2 <= qb) AT_LOAD_TILE(grp + 2);
;         asm volatile("s_waitcnt lgkmcnt(0)" ::: "memory"); __builtin_amdgcn_s_barrier(); asm volatile("" ::: "memory");
.LBB0_543:
	s_and_b64 s[4:5], s[2:3], exec
	v_readlane_b32 s0, v253, 26
	v_readlane_b32 s1, v253, 27
	s_cselect_b32 s10, s1, s0
	s_lshl_b32 s14, s10, 5
	v_or_b32_e32 v0, s14, v220
	v_readlane_b32 s0, v253, 38
	s_nop 1
	v_or_b32_e32 v208, s0, v0
	v_mov_b64_e32 v[0:1], s[96:97]
	v_mad_i64_i32 v[0:1], s[4:5], v208, s94, v[0:1]
	v_readlane_b32 s0, v255, 10
	s_mov_b32 s4, s0
	s_mov_b32 s5, s63
	v_lshl_add_u64 v[0:1], v[0:1], 0, s[4:5]
	v_lshl_add_u64 v[0:1], v[0:1], 0, v[192:193]
	v_lshl_add_u64 v[2:3], v[0:1], 0, s[52:53]
	v_add_co_u32_e32 v0, vcc, s95, v0
	v_readlane_b32 s1, v255, 11
	s_nop 0
	v_addc_co_u32_e32 v1, vcc, 0, v1, vcc
	global_load_dwordx4 v[112:115], v[2:3], off offset:32 nt
	global_load_dwordx4 v[116:119], v[2:3], off offset:64 nt
	global_load_dwordx4 v[120:123], v[2:3], off offset:96 nt
	global_load_dwordx4 v[124:127], v[2:3], off offset:128 nt
	global_load_dwordx4 v[128:131], v[2:3], off offset:160 nt
	global_load_dwordx4 v[132:135], v[2:3], off offset:192 nt
	global_load_dwordx4 v[136:139], v[0:1], off nt
	global_load_dwordx4 v[140:143], v[2:3], off offset:224 nt
	v_mov_b32_e32 v0, s9
	ds_read_b32 v211, v0 offset:512
	v_writelane_b32 v255, s0, 10
	v_ashrrev_i32_e32 v209, 31, v208
	v_lshlrev_b64 v[18:19], 8, v[208:209]
	v_writelane_b32 v255, s1, 11
	v_readlane_b32 s0, v253, 31
	s_cmp_le_u32 s0, s10
	s_mov_b64 s[4:5], -1
	s_cbranch_scc0 .LBB0_545
	v_readlane_b32 s0, v253, 28
	v_lshlrev_b64 v[16:17], 8, v[208:209]
	v_readlane_b32 s1, v253, 29
	v_add_u32_e32 v22, 0x8800, v225
	s_mov_b64 s[4:5], 0
	v_lshl_add_u64 v[0:1], s[0:1], 0, v[16:17]
	global_load_dword v229, v[0:1], off
	global_load_dwordx4 v[0:3], v[178:179], off
	global_load_dwordx4 v[4:7], v[180:181], off
	global_load_dwordx4 v[8:11], v[182:183], off
	global_load_dwordx4 v[12:15], v[184:185], off
	s_waitcnt vmcnt(3)
	ds_write_b128 v228, v[0:3]
	s_waitcnt vmcnt(2)
	ds_write_b128 v228, v[4:7] offset:4352
	s_waitcnt vmcnt(1)
	v_and_b32_e32 v20, 0xffff, v8
	v_lshrrev_b32_e32 v21, 16, v8
	s_waitcnt vmcnt(0)
	v_lshl_or_b32 v20, v12, 16, v20
	v_and_or_b32 v21, v12, s92, v21
	ds_write2_b32 v22, v20, v21 offset1:18
	v_and_b32_e32 v20, 0xffff, v9
	v_lshrrev_b32_e32 v21, 16, v9
	v_lshl_or_b32 v20, v13, 16, v20
	v_and_or_b32 v21, v13, s92, v21
	ds_write2_b32 v22, v20, v21 offset0:36 offset1:54
	v_and_b32_e32 v20, 0xffff, v10
	v_lshrrev_b32_e32 v21, 16, v10
	v_lshl_or_b32 v20, v14, 16, v20
	v_and_or_b32 v21, v14, s92, v21
	ds_write2_b32 v22, v20, v21 offset0:72 offset1:90
	v_and_b32_e32 v20, 0xffff, v11
	v_lshrrev_b32_e32 v21, 16, v11
	v_lshl_or_b32 v20, v15, 16, v20
	v_and_or_b32 v21, v15, s92, v21
	ds_write2_b32 v22, v20, v21 offset0:108 offset1:126
